# baseline (speedup 1.0000x reference)
_Z11edge_kernelILi64ELb0EEvPKfS1_PKDF16_PKiS5_S1_S1_S1_S1_S1_PDF16_:
	s_load_dwordx16 s[4:19], s[0:1], 0x10
	s_load_dwordx2 s[20:21], s[0:1], 0x50
	v_readfirstlane_b32 s3, v0
	v_bfe_u32 v75, v0, 4, 2
	v_and_b32_e32 v76, 15, v0
	v_and_b32_e32 v78, 63, v0
	s_lshr_b32 s3, s3, 6
	s_lshl_b32 s2, s2, 1
	s_add_i32 s2, s2, s3
	v_lshlrev_b32_e32 v74, 8, v75
	v_lshl_or_b32 v74, v76, 4, v74
	v_lshlrev_b32_e32 v79, 4, v78
	v_lshl_or_b32 v77, v76, 2, v75
	v_lshlrev_b32_e32 v77, 2, v77
	v_lshlrev_b32_e32 v78, 5, v75
	v_lshlrev_b32_e32 v73, 12, v75
	v_lshl_or_b32 v73, v76, 4, v73
	s_lshl_b32 s28, s2, 14
	s_lshl_b32 s29, s2, 14
	s_lshl_b32 s30, s2, 2
	s_lshl_b32 s31, s2, 8
	s_lshl_b32 s33, s3, 10
	s_lshl_b32 s34, s3, 8
	s_addk_i32 s34, 0x4000
	s_waitcnt lgkmcnt(0)
	s_add_u32 s6, s6, s30
	s_addc_u32 s7, s7, 0
	s_add_u32 s8, s8, s30
	s_addc_u32 s9, s9, 0
	s_load_dword s35, s[6:7], 0x0
	s_load_dword s36, s[8:9], 0x0
	s_add_u32 s10, s10, s28
	s_addc_u32 s11, s11, 0
	s_add_u32 s18, s18, s33
	s_addc_u32 s19, s19, 0
	s_add_u32 s14, s14, s29
	s_addc_u32 s15, s15, 0
	s_add_u32 s12, s12, s31
	s_addc_u32 s13, s13, 0
	s_add_u32 s16, s16, s31
	s_addc_u32 s17, s17, 0
	s_waitcnt lgkmcnt(0)
	s_lshl_b32 s36, s36, 7
	s_add_u32 s20, s20, s36
	s_addc_u32 s21, s21, 0
	s_lshl_b32 s37, s35, 7
	s_add_u32 s4, s4, s37
	s_addc_u32 s5, s5, 0
	global_load_dwordx4 v[64:67], v78, s[4:5] nt
	global_load_dwordx4 v[68:71], v78, s[4:5] offset:16 nt
	v_add_u32_e32 v78, s34, v77
	v_lshlrev_b32_e32 v96, 12, v75
	v_lshl_or_b32 v96, v76, 4, v96
	s_cmpk_ge_u32 s2, 0x2510
	s_cbranch_scc0 .Le2_wait_gather
	global_load_dwordx4 v[0:3], v96, s[10:11] nt
	global_load_dwordx4 v[4:7], v96, s[10:11] offset:256 nt
	global_load_dwordx4 v[8:11], v96, s[10:11] offset:512 nt
	global_load_dwordx4 v[12:15], v96, s[10:11] offset:768 nt
	global_load_dwordx4 v[16:19], v96, s[10:11] offset:1024 nt
	global_load_dwordx4 v[20:23], v96, s[10:11] offset:1280 nt
	global_load_dwordx4 v[24:27], v96, s[10:11] offset:1536 nt
	global_load_dwordx4 v[28:31], v96, s[10:11] offset:1792 nt
	global_load_dwordx4 v[32:35], v96, s[10:11] offset:2048 nt
	global_load_dwordx4 v[36:39], v96, s[10:11] offset:2304 nt
	global_load_dwordx4 v[40:43], v96, s[10:11] offset:2560 nt
	global_load_dwordx4 v[44:47], v96, s[10:11] offset:2816 nt
	global_load_dwordx4 v[48:51], v96, s[10:11] offset:3072 nt
	global_load_dwordx4 v[52:55], v96, s[10:11] offset:3328 nt
	global_load_dwordx4 v[56:59], v96, s[10:11] offset:3584 nt
	global_load_dwordx4 v[60:63], v96, s[10:11] offset:3840 nt
	s_waitcnt vmcnt(16)
	s_branch .Le2_cvt
.Le2_wait_gather:
	s_waitcnt vmcnt(0)
.Le2_cvt:
	v_cvt_f32_f16_e32 v80, v64
	v_cvt_f32_f16_sdwa v81, v64 dst_sel:DWORD dst_unused:UNUSED_PAD src0_sel:WORD_1
	v_cvt_f32_f16_e32 v82, v65
	v_cvt_f32_f16_sdwa v83, v65 dst_sel:DWORD dst_unused:UNUSED_PAD src0_sel:WORD_1
	v_cvt_f32_f16_e32 v84, v66
	v_cvt_f32_f16_sdwa v85, v66 dst_sel:DWORD dst_unused:UNUSED_PAD src0_sel:WORD_1
	v_cvt_f32_f16_e32 v86, v67
	v_cvt_f32_f16_sdwa v87, v67 dst_sel:DWORD dst_unused:UNUSED_PAD src0_sel:WORD_1
	v_cvt_f32_f16_e32 v88, v68
	v_cvt_f32_f16_sdwa v89, v68 dst_sel:DWORD dst_unused:UNUSED_PAD src0_sel:WORD_1
	v_cvt_f32_f16_e32 v90, v69
	v_cvt_f32_f16_sdwa v91, v69 dst_sel:DWORD dst_unused:UNUSED_PAD src0_sel:WORD_1
	v_cvt_f32_f16_e32 v92, v70
	v_cvt_f32_f16_sdwa v93, v70 dst_sel:DWORD dst_unused:UNUSED_PAD src0_sel:WORD_1
	v_cvt_f32_f16_e32 v94, v71
	v_cvt_f32_f16_sdwa v95, v71 dst_sel:DWORD dst_unused:UNUSED_PAD src0_sel:WORD_1
	v_max_f32_e32 v80, 0, v80
	v_max_f32_e32 v81, 0, v81
	v_max_f32_e32 v82, 0, v82
	v_max_f32_e32 v83, 0, v83
	v_max_f32_e32 v84, 0, v84
	v_max_f32_e32 v85, 0, v85
	v_max_f32_e32 v86, 0, v86
	v_max_f32_e32 v87, 0, v87
	v_max_f32_e32 v88, 0, v88
	v_max_f32_e32 v89, 0, v89
	v_max_f32_e32 v90, 0, v90
	v_max_f32_e32 v91, 0, v91
	v_max_f32_e32 v92, 0, v92
	v_max_f32_e32 v93, 0, v93
	v_max_f32_e32 v94, 0, v94
	v_max_f32_e32 v95, 0, v95
	v_cmp_neq_f32_e64 s[40:41], 0, v80
	v_cmp_neq_f32_e64 s[42:43], 0, v81
	v_cmp_neq_f32_e64 s[44:45], 0, v82
	v_cmp_neq_f32_e64 s[46:47], 0, v83
	v_cmp_neq_f32_e64 s[48:49], 0, v84
	v_cmp_neq_f32_e64 s[50:51], 0, v85
	v_cmp_neq_f32_e64 s[52:53], 0, v86
	v_cmp_neq_f32_e64 s[54:55], 0, v87
	v_cmp_neq_f32_e64 s[56:57], 0, v88
	v_cmp_neq_f32_e64 s[58:59], 0, v89
	v_cmp_neq_f32_e64 s[60:61], 0, v90
	v_cmp_neq_f32_e64 s[62:63], 0, v91
	v_cmp_neq_f32_e64 s[64:65], 0, v92
	v_cmp_neq_f32_e64 s[66:67], 0, v93
	v_cmp_neq_f32_e64 s[68:69], 0, v94
	v_cmp_neq_f32_e64 s[70:71], 0, v95
	s_cmpk_ge_u32 s2, 0x2510
	s_cbranch_scc1 .Le2_w1_issued
	s_mov_b64 exec, s[40:41]
	global_load_dwordx4 v[0:3], v96, s[10:11] nt
	s_mov_b64 exec, s[42:43]
	global_load_dwordx4 v[4:7], v96, s[10:11] offset:256 nt
	s_mov_b64 exec, s[44:45]
	global_load_dwordx4 v[8:11], v96, s[10:11] offset:512 nt
	s_mov_b64 exec, s[46:47]
	global_load_dwordx4 v[12:15], v96, s[10:11] offset:768 nt
	s_mov_b64 exec, s[48:49]
	global_load_dwordx4 v[16:19], v96, s[10:11] offset:1024 nt
	s_mov_b64 exec, s[50:51]
	global_load_dwordx4 v[20:23], v96, s[10:11] offset:1280 nt
	s_mov_b64 exec, s[52:53]
	global_load_dwordx4 v[24:27], v96, s[10:11] offset:1536 nt
	s_mov_b64 exec, s[54:55]
	global_load_dwordx4 v[28:31], v96, s[10:11] offset:1792 nt
	s_mov_b64 exec, s[56:57]
	global_load_dwordx4 v[32:35], v96, s[10:11] offset:2048 nt
	s_mov_b64 exec, s[58:59]
	global_load_dwordx4 v[36:39], v96, s[10:11] offset:2304 nt
	s_mov_b64 exec, s[60:61]
	global_load_dwordx4 v[40:43], v96, s[10:11] offset:2560 nt
	s_mov_b64 exec, s[62:63]
	global_load_dwordx4 v[44:47], v96, s[10:11] offset:2816 nt
	s_mov_b64 exec, s[64:65]
	global_load_dwordx4 v[48:51], v96, s[10:11] offset:3072 nt
	s_mov_b64 exec, s[66:67]
	global_load_dwordx4 v[52:55], v96, s[10:11] offset:3328 nt
	s_mov_b64 exec, s[68:69]
	global_load_dwordx4 v[56:59], v96, s[10:11] offset:3584 nt
	s_mov_b64 exec, s[70:71]
	global_load_dwordx4 v[60:63], v96, s[10:11] offset:3840 nt
.Le2_w1_issued:
	s_mov_b64 exec, -1
	s_mov_b32 m0, s33
	s_nop 0
	global_load_lds_dwordx4 v79, s[18:19]
	global_load_lds_dwordx4 v79, s[18:19] offset:2048
	s_add_u32 m0, m0, 0x1000
	s_add_u32 s18, s18, 0x1000
	s_addc_u32 s19, s19, 0
	global_load_lds_dwordx4 v79, s[18:19]
	global_load_lds_dwordx4 v79, s[18:19] offset:2048
	s_add_u32 m0, m0, 0x1000
	s_add_u32 s18, s18, 0x1000
	s_addc_u32 s19, s19, 0
	global_load_lds_dwordx4 v79, s[18:19]
	global_load_lds_dwordx4 v79, s[18:19] offset:2048
	s_add_u32 m0, m0, 0x1000
	s_add_u32 s18, s18, 0x1000
	s_addc_u32 s19, s19, 0
	global_load_lds_dwordx4 v79, s[18:19]
	global_load_lds_dwordx4 v79, s[18:19] offset:2048
	global_load_dword v72, v77, s[12:13] nt
	global_load_dword v73, v77, s[16:17] nt
	v_lshl_add_u32 v79, v75, 2, s34
	v_mov_b32_e32 v96, 0
	v_mov_b32_e32 v97, 0
	v_mov_b32_e32 v98, 0
	v_mov_b32_e32 v99, 0
	v_mov_b32_e32 v100, 0
	v_mov_b32_e32 v101, 0
	v_mov_b32_e32 v102, 0
	v_mov_b32_e32 v103, 0
	s_waitcnt vmcnt(0)
	s_barrier
	s_mov_b64 exec, s[40:41]
	v_pk_fma_f32 v[96:97], v[80:81], v[0:1], v[96:97] op_sel_hi:[0,1,1]
	v_pk_fma_f32 v[98:99], v[80:81], v[2:3], v[98:99] op_sel_hi:[0,1,1]
	s_mov_b64 exec, s[42:43]
	v_pk_fma_f32 v[100:101], v[80:81], v[4:5], v[100:101] op_sel:[1,0,0]
	v_pk_fma_f32 v[102:103], v[80:81], v[6:7], v[102:103] op_sel:[1,0,0]
	s_mov_b64 exec, s[44:45]
	v_pk_fma_f32 v[96:97], v[82:83], v[8:9], v[96:97] op_sel_hi:[0,1,1]
	v_pk_fma_f32 v[98:99], v[82:83], v[10:11], v[98:99] op_sel_hi:[0,1,1]
	s_mov_b64 exec, s[46:47]
	v_pk_fma_f32 v[100:101], v[82:83], v[12:13], v[100:101] op_sel:[1,0,0]
	v_pk_fma_f32 v[102:103], v[82:83], v[14:15], v[102:103] op_sel:[1,0,0]
	s_mov_b64 exec, s[48:49]
	v_pk_fma_f32 v[96:97], v[84:85], v[16:17], v[96:97] op_sel_hi:[0,1,1]
	v_pk_fma_f32 v[98:99], v[84:85], v[18:19], v[98:99] op_sel_hi:[0,1,1]
	s_mov_b64 exec, s[50:51]
	v_pk_fma_f32 v[100:101], v[84:85], v[20:21], v[100:101] op_sel:[1,0,0]
	v_pk_fma_f32 v[102:103], v[84:85], v[22:23], v[102:103] op_sel:[1,0,0]
	s_mov_b64 exec, s[52:53]
	v_pk_fma_f32 v[96:97], v[86:87], v[24:25], v[96:97] op_sel_hi:[0,1,1]
	v_pk_fma_f32 v[98:99], v[86:87], v[26:27], v[98:99] op_sel_hi:[0,1,1]
	s_mov_b64 exec, s[54:55]
	v_pk_fma_f32 v[100:101], v[86:87], v[28:29], v[100:101] op_sel:[1,0,0]
	v_pk_fma_f32 v[102:103], v[86:87], v[30:31], v[102:103] op_sel:[1,0,0]
	s_mov_b64 exec, s[56:57]
	v_pk_fma_f32 v[96:97], v[88:89], v[32:33], v[96:97] op_sel_hi:[0,1,1]
	v_pk_fma_f32 v[98:99], v[88:89], v[34:35], v[98:99] op_sel_hi:[0,1,1]
	s_mov_b64 exec, s[58:59]
	v_pk_fma_f32 v[100:101], v[88:89], v[36:37], v[100:101] op_sel:[1,0,0]
	v_pk_fma_f32 v[102:103], v[88:89], v[38:39], v[102:103] op_sel:[1,0,0]
	s_mov_b64 exec, s[60:61]
	v_pk_fma_f32 v[96:97], v[90:91], v[40:41], v[96:97] op_sel_hi:[0,1,1]
	v_pk_fma_f32 v[98:99], v[90:91], v[42:43], v[98:99] op_sel_hi:[0,1,1]
	s_mov_b64 exec, s[62:63]
	v_pk_fma_f32 v[100:101], v[90:91], v[44:45], v[100:101] op_sel:[1,0,0]
	v_pk_fma_f32 v[102:103], v[90:91], v[46:47], v[102:103] op_sel:[1,0,0]
	s_mov_b64 exec, s[64:65]
	v_pk_fma_f32 v[96:97], v[92:93], v[48:49], v[96:97] op_sel_hi:[0,1,1]
	v_pk_fma_f32 v[98:99], v[92:93], v[50:51], v[98:99] op_sel_hi:[0,1,1]
	s_mov_b64 exec, s[66:67]
	v_pk_fma_f32 v[100:101], v[92:93], v[52:53], v[100:101] op_sel:[1,0,0]
	v_pk_fma_f32 v[102:103], v[92:93], v[54:55], v[102:103] op_sel:[1,0,0]
	s_mov_b64 exec, s[68:69]
	v_pk_fma_f32 v[96:97], v[94:95], v[56:57], v[96:97] op_sel_hi:[0,1,1]
	v_pk_fma_f32 v[98:99], v[94:95], v[58:59], v[98:99] op_sel_hi:[0,1,1]
	s_mov_b64 exec, s[70:71]
	v_pk_fma_f32 v[100:101], v[94:95], v[60:61], v[100:101] op_sel:[1,0,0]
	v_pk_fma_f32 v[102:103], v[94:95], v[62:63], v[102:103] op_sel:[1,0,0]
	s_mov_b64 exec, -1
	v_pk_add_f32 v[96:97], v[96:97], v[100:101]
	v_pk_add_f32 v[98:99], v[98:99], v[102:103]
	s_nop 1
	v_permlane16_swap_b32_e32 v96, v97
	v_permlane16_swap_b32_e32 v98, v99
	v_add_f32_e32 v96, v96, v97
	v_add_f32_e32 v98, v98, v99
	s_nop 1
	v_permlane32_swap_b32_e32 v96, v98
	v_add_f32_e32 v96, v96, v98
	s_waitcnt vmcnt(1)
	v_add_f32_e32 v96, v96, v72
	v_max_f32_e32 v96, 0, v96
	ds_write_b32 v78, v96
	ds_read2_b32 v[80:81], v79 offset0:0 offset1:4
	ds_read2_b32 v[82:83], v79 offset0:8 offset1:12
	ds_read2_b32 v[84:85], v79 offset0:16 offset1:20
	ds_read2_b32 v[86:87], v79 offset0:24 offset1:28
	ds_read2_b32 v[88:89], v79 offset0:32 offset1:36
	ds_read2_b32 v[90:91], v79 offset0:40 offset1:44
	ds_read2_b32 v[92:93], v79 offset0:48 offset1:52
	ds_read2_b32 v[94:95], v79 offset0:56 offset1:60
	s_waitcnt lgkmcnt(0)
	v_cmp_neq_f32_e64 s[40:41], 0, v80
	v_cmp_neq_f32_e64 s[42:43], 0, v81
	v_cmp_neq_f32_e64 s[44:45], 0, v82
	v_cmp_neq_f32_e64 s[46:47], 0, v83
	v_cmp_neq_f32_e64 s[48:49], 0, v84
	v_cmp_neq_f32_e64 s[50:51], 0, v85
	v_cmp_neq_f32_e64 s[52:53], 0, v86
	v_cmp_neq_f32_e64 s[54:55], 0, v87
	v_cmp_neq_f32_e64 s[56:57], 0, v88
	v_cmp_neq_f32_e64 s[58:59], 0, v89
	v_cmp_neq_f32_e64 s[60:61], 0, v90
	v_cmp_neq_f32_e64 s[62:63], 0, v91
	v_cmp_neq_f32_e64 s[64:65], 0, v92
	v_cmp_neq_f32_e64 s[66:67], 0, v93
	v_cmp_neq_f32_e64 s[68:69], 0, v94
	v_cmp_neq_f32_e64 s[70:71], 0, v95
	s_mov_b64 exec, s[40:41]
	global_load_dwordx4 v[0:3], v74, s[14:15] nt
	s_mov_b64 exec, s[42:43]
	global_load_dwordx4 v[4:7], v74, s[14:15] offset:1024 nt
	s_mov_b64 exec, s[44:45]
	global_load_dwordx4 v[8:11], v74, s[14:15] offset:2048 nt
	s_mov_b64 exec, s[46:47]
	global_load_dwordx4 v[12:15], v74, s[14:15] offset:3072 nt
	s_add_u32 s14, s14, 0x1000
	s_addc_u32 s15, s15, 0
	s_mov_b64 exec, s[48:49]
	global_load_dwordx4 v[16:19], v74, s[14:15] nt
	s_mov_b64 exec, s[50:51]
	global_load_dwordx4 v[20:23], v74, s[14:15] offset:1024 nt
	s_mov_b64 exec, s[52:53]
	global_load_dwordx4 v[24:27], v74, s[14:15] offset:2048 nt
	s_mov_b64 exec, s[54:55]
	global_load_dwordx4 v[28:31], v74, s[14:15] offset:3072 nt
	s_add_u32 s14, s14, 0x1000
	s_addc_u32 s15, s15, 0
	s_mov_b64 exec, s[56:57]
	global_load_dwordx4 v[32:35], v74, s[14:15] nt
	s_mov_b64 exec, s[58:59]
	global_load_dwordx4 v[36:39], v74, s[14:15] offset:1024 nt
	s_mov_b64 exec, s[60:61]
	global_load_dwordx4 v[40:43], v74, s[14:15] offset:2048 nt
	s_mov_b64 exec, s[62:63]
	global_load_dwordx4 v[44:47], v74, s[14:15] offset:3072 nt
	s_add_u32 s14, s14, 0x1000
	s_addc_u32 s15, s15, 0
	s_mov_b64 exec, s[64:65]
	global_load_dwordx4 v[48:51], v74, s[14:15] nt
	s_mov_b64 exec, s[66:67]
	global_load_dwordx4 v[52:55], v74, s[14:15] offset:1024 nt
	s_mov_b64 exec, s[68:69]
	global_load_dwordx4 v[56:59], v74, s[14:15] offset:2048 nt
	s_mov_b64 exec, s[70:71]
	global_load_dwordx4 v[60:63], v74, s[14:15] offset:3072 nt
	s_mov_b64 exec, -1
	v_mov_b32_e32 v96, 0
	v_mov_b32_e32 v97, 0
	v_mov_b32_e32 v98, 0
	v_mov_b32_e32 v99, 0
	v_mov_b32_e32 v100, 0
	v_mov_b32_e32 v101, 0
	v_mov_b32_e32 v102, 0
	v_mov_b32_e32 v103, 0
	s_waitcnt vmcnt(0)
	s_mov_b64 exec, s[40:41]
	v_pk_fma_f32 v[96:97], v[80:81], v[0:1], v[96:97] op_sel_hi:[0,1,1]
	v_pk_fma_f32 v[98:99], v[80:81], v[2:3], v[98:99] op_sel_hi:[0,1,1]
	s_mov_b64 exec, s[42:43]
	v_pk_fma_f32 v[100:101], v[80:81], v[4:5], v[100:101] op_sel:[1,0,0]
	v_pk_fma_f32 v[102:103], v[80:81], v[6:7], v[102:103] op_sel:[1,0,0]
	s_mov_b64 exec, s[44:45]
	v_pk_fma_f32 v[96:97], v[82:83], v[8:9], v[96:97] op_sel_hi:[0,1,1]
	v_pk_fma_f32 v[98:99], v[82:83], v[10:11], v[98:99] op_sel_hi:[0,1,1]
	s_mov_b64 exec, s[46:47]
	v_pk_fma_f32 v[100:101], v[82:83], v[12:13], v[100:101] op_sel:[1,0,0]
	v_pk_fma_f32 v[102:103], v[82:83], v[14:15], v[102:103] op_sel:[1,0,0]
	s_mov_b64 exec, s[48:49]
	v_pk_fma_f32 v[96:97], v[84:85], v[16:17], v[96:97] op_sel_hi:[0,1,1]
	v_pk_fma_f32 v[98:99], v[84:85], v[18:19], v[98:99] op_sel_hi:[0,1,1]
	s_mov_b64 exec, s[50:51]
	v_pk_fma_f32 v[100:101], v[84:85], v[20:21], v[100:101] op_sel:[1,0,0]
	v_pk_fma_f32 v[102:103], v[84:85], v[22:23], v[102:103] op_sel:[1,0,0]
	s_mov_b64 exec, s[52:53]
	v_pk_fma_f32 v[96:97], v[86:87], v[24:25], v[96:97] op_sel_hi:[0,1,1]
	v_pk_fma_f32 v[98:99], v[86:87], v[26:27], v[98:99] op_sel_hi:[0,1,1]
	s_mov_b64 exec, s[54:55]
	v_pk_fma_f32 v[100:101], v[86:87], v[28:29], v[100:101] op_sel:[1,0,0]
	v_pk_fma_f32 v[102:103], v[86:87], v[30:31], v[102:103] op_sel:[1,0,0]
	s_mov_b64 exec, s[56:57]
	v_pk_fma_f32 v[96:97], v[88:89], v[32:33], v[96:97] op_sel_hi:[0,1,1]
	v_pk_fma_f32 v[98:99], v[88:89], v[34:35], v[98:99] op_sel_hi:[0,1,1]
	s_mov_b64 exec, s[58:59]
	v_pk_fma_f32 v[100:101], v[88:89], v[36:37], v[100:101] op_sel:[1,0,0]
	v_pk_fma_f32 v[102:103], v[88:89], v[38:39], v[102:103] op_sel:[1,0,0]
	s_mov_b64 exec, s[60:61]
	v_pk_fma_f32 v[96:97], v[90:91], v[40:41], v[96:97] op_sel_hi:[0,1,1]
	v_pk_fma_f32 v[98:99], v[90:91], v[42:43], v[98:99] op_sel_hi:[0,1,1]
	s_mov_b64 exec, s[62:63]
	v_pk_fma_f32 v[100:101], v[90:91], v[44:45], v[100:101] op_sel:[1,0,0]
	v_pk_fma_f32 v[102:103], v[90:91], v[46:47], v[102:103] op_sel:[1,0,0]
	s_mov_b64 exec, s[64:65]
	v_pk_fma_f32 v[96:97], v[92:93], v[48:49], v[96:97] op_sel_hi:[0,1,1]
	v_pk_fma_f32 v[98:99], v[92:93], v[50:51], v[98:99] op_sel_hi:[0,1,1]
	s_mov_b64 exec, s[66:67]
	v_pk_fma_f32 v[100:101], v[92:93], v[52:53], v[100:101] op_sel:[1,0,0]
	v_pk_fma_f32 v[102:103], v[92:93], v[54:55], v[102:103] op_sel:[1,0,0]
	s_mov_b64 exec, s[68:69]
	v_pk_fma_f32 v[96:97], v[94:95], v[56:57], v[96:97] op_sel_hi:[0,1,1]
	v_pk_fma_f32 v[98:99], v[94:95], v[58:59], v[98:99] op_sel_hi:[0,1,1]
	s_mov_b64 exec, s[70:71]
	v_pk_fma_f32 v[100:101], v[94:95], v[60:61], v[100:101] op_sel:[1,0,0]
	v_pk_fma_f32 v[102:103], v[94:95], v[62:63], v[102:103] op_sel:[1,0,0]
	s_mov_b64 exec, -1
	ds_read_b128 v[0:3], v74
	ds_read_b128 v[4:7], v74 offset:1024
	ds_read_b128 v[8:11], v74 offset:2048
	ds_read_b128 v[12:15], v74 offset:3072
	ds_read_b128 v[16:19], v74 offset:4096
	ds_read_b128 v[20:23], v74 offset:5120
	ds_read_b128 v[24:27], v74 offset:6144
	ds_read_b128 v[28:31], v74 offset:7168
	ds_read_b128 v[32:35], v74 offset:8192
	ds_read_b128 v[36:39], v74 offset:9216
	ds_read_b128 v[40:43], v74 offset:10240
	ds_read_b128 v[44:47], v74 offset:11264
	ds_read_b128 v[48:51], v74 offset:12288
	ds_read_b128 v[52:55], v74 offset:13312
	ds_read_b128 v[56:59], v74 offset:14336
	v_pk_add_f32 v[96:97], v[96:97], v[100:101]
	v_pk_add_f32 v[98:99], v[98:99], v[102:103]
	s_nop 1
	v_permlane16_swap_b32_e32 v96, v97
	v_permlane16_swap_b32_e32 v98, v99
	v_add_f32_e32 v96, v96, v97
	v_add_f32_e32 v98, v98, v99
	s_nop 1
	v_permlane32_swap_b32_e32 v96, v98
	v_add_f32_e32 v96, v96, v98
	v_add_f32_e32 v96, v96, v73
	s_waitcnt lgkmcnt(5)
	ds_read_b128 v[60:63], v74 offset:15360
	ds_write_b32 v78, v96
	ds_read2_b32 v[80:81], v79 offset0:0 offset1:4
	ds_read2_b32 v[82:83], v79 offset0:8 offset1:12
	ds_read2_b32 v[84:85], v79 offset0:16 offset1:20
	ds_read2_b32 v[86:87], v79 offset0:24 offset1:28
	ds_read2_b32 v[88:89], v79 offset0:32 offset1:36
	ds_read2_b32 v[90:91], v79 offset0:40 offset1:44
	ds_read2_b32 v[92:93], v79 offset0:48 offset1:52
	ds_read2_b32 v[94:95], v79 offset0:56 offset1:60
	v_lshlrev_b32_e32 v72, 3, v76
	v_lshl_or_b32 v72, v75, 2, v72
	v_cmp_gt_u32_e32 vcc, 2, v75
	s_waitcnt lgkmcnt(0)
	v_pk_mul_f32 v[96:97], v[80:81], v[0:1] op_sel_hi:[0,1]
	v_pk_mul_f32 v[98:99], v[80:81], v[2:3] op_sel_hi:[0,1]
	v_pk_mul_f32 v[100:101], v[80:81], v[4:5] op_sel:[1,0]
	v_pk_mul_f32 v[102:103], v[80:81], v[6:7] op_sel:[1,0]
	v_pk_fma_f32 v[96:97], v[82:83], v[8:9], v[96:97] op_sel_hi:[0,1,1]
	v_pk_fma_f32 v[98:99], v[82:83], v[10:11], v[98:99] op_sel_hi:[0,1,1]
	v_pk_fma_f32 v[100:101], v[82:83], v[12:13], v[100:101] op_sel:[1,0,0]
	v_pk_fma_f32 v[102:103], v[82:83], v[14:15], v[102:103] op_sel:[1,0,0]
	v_pk_fma_f32 v[96:97], v[84:85], v[16:17], v[96:97] op_sel_hi:[0,1,1]
	v_pk_fma_f32 v[98:99], v[84:85], v[18:19], v[98:99] op_sel_hi:[0,1,1]
	v_pk_fma_f32 v[100:101], v[84:85], v[20:21], v[100:101] op_sel:[1,0,0]
	v_pk_fma_f32 v[102:103], v[84:85], v[22:23], v[102:103] op_sel:[1,0,0]
	v_pk_fma_f32 v[96:97], v[86:87], v[24:25], v[96:97] op_sel_hi:[0,1,1]
	v_pk_fma_f32 v[98:99], v[86:87], v[26:27], v[98:99] op_sel_hi:[0,1,1]
	v_pk_fma_f32 v[100:101], v[86:87], v[28:29], v[100:101] op_sel:[1,0,0]
	v_pk_fma_f32 v[102:103], v[86:87], v[30:31], v[102:103] op_sel:[1,0,0]
	v_pk_fma_f32 v[96:97], v[88:89], v[32:33], v[96:97] op_sel_hi:[0,1,1]
	v_pk_fma_f32 v[98:99], v[88:89], v[34:35], v[98:99] op_sel_hi:[0,1,1]
	v_pk_fma_f32 v[100:101], v[88:89], v[36:37], v[100:101] op_sel:[1,0,0]
	v_pk_fma_f32 v[102:103], v[88:89], v[38:39], v[102:103] op_sel:[1,0,0]
	v_pk_fma_f32 v[96:97], v[90:91], v[40:41], v[96:97] op_sel_hi:[0,1,1]
	v_pk_fma_f32 v[98:99], v[90:91], v[42:43], v[98:99] op_sel_hi:[0,1,1]
	v_pk_fma_f32 v[100:101], v[90:91], v[44:45], v[100:101] op_sel:[1,0,0]
	v_pk_fma_f32 v[102:103], v[90:91], v[46:47], v[102:103] op_sel:[1,0,0]
	v_pk_fma_f32 v[96:97], v[92:93], v[48:49], v[96:97] op_sel_hi:[0,1,1]
	v_pk_fma_f32 v[98:99], v[92:93], v[50:51], v[98:99] op_sel_hi:[0,1,1]
	v_pk_fma_f32 v[100:101], v[92:93], v[52:53], v[100:101] op_sel:[1,0,0]
	v_pk_fma_f32 v[102:103], v[92:93], v[54:55], v[102:103] op_sel:[1,0,0]
	v_pk_fma_f32 v[96:97], v[94:95], v[56:57], v[96:97] op_sel_hi:[0,1,1]
	v_pk_fma_f32 v[98:99], v[94:95], v[58:59], v[98:99] op_sel_hi:[0,1,1]
	v_pk_fma_f32 v[100:101], v[94:95], v[60:61], v[100:101] op_sel:[1,0,0]
	v_pk_fma_f32 v[102:103], v[94:95], v[62:63], v[102:103] op_sel:[1,0,0]
	v_pk_add_f32 v[96:97], v[96:97], v[100:101]
	v_pk_add_f32 v[98:99], v[98:99], v[102:103]
	s_nop 1
	v_permlane16_swap_b32_e32 v96, v98
	v_permlane16_swap_b32_e32 v97, v99
	v_add_f32_e32 v96, v96, v98
	v_add_f32_e32 v97, v97, v99
	v_mov_b32_e32 v80, v96
	v_mov_b32_e32 v81, v97
	s_nop 1
	v_permlane32_swap_b32_e32 v96, v80
	v_permlane32_swap_b32_e32 v97, v81
	v_add_f32_e32 v96, v96, v80
	v_add_f32_e32 v97, v97, v81
	v_cvt_pk_f16_f32 v73, v96, v97
	s_and_saveexec_b64 s[4:5], vcc
	global_atomic_pk_add_f16 v72, v73, s[20:21]
	s_endpgm
	.p2align	8
